# norm1 phase: the per-token vector load of the residual base pointer (dependent round trip + vmcnt drain per token) replaced by two scalar loads before the loop and a v_cndmask select
# speedup vs baseline: 1.0062x; 1.0062x over previous
; #define LAS __attribute__((address_space(3)))
;     template <class T> __device__ __forceinline__ T* w(size_t off) const { return (T*)(p->ws + off); }
; __device__ __forceinline__ void ph_norm1(const Ctx& c, int layer, int gw, int nwaves, unsigned char* lds) {
;     const int lane = c.tid & 63;
;     bf16* HA = c.w<bf16>(WS_HA); float* DTR = c.w<float>(WS_DTR);
;     const float* MOD = c.w<float>(WS_MOD) + (size_t)layer * 5 * 6144;
;     const float* g = c.in(6) + layer * D;
;     __syncthreads();
;     {
;         f32x4 w8[8];
; #pragma unroll
;         for (int j = 0; j < 8; ++j) w8[j] = ((const f32x4*)(c.w<float>(WS_WDT) + (size_t)layer * 8 * 1024))[c.tid + NTHR * j];
; #pragma unroll
;         for (int j = 0; j < 8; ++j) ((LAS f32x4*)lds)[c.tid + NTHR * j] = w8[j];
;     }
;     __syncthreads();
;     const LAS float* wdt = (const LAS float*)lds;
;     f32x4 gv[4];
; #pragma unroll
;     for (int i = 0; i < 4; ++i) gv[i] = *(const f32x4*)(g + (lane + 64 * i) * 4);
;     for (int n = gw; n < NT; n += nwaves) {
;         const int b = n / LT, pos = n % LT, mr = pos < CTX ? 4 : b;
;         const float* x = xsrc(c, layer, n);
.Lstag_n1:
.Lstag_done:
	s_mov_b64 s[4:5], s[0:1]
	v_mov_b32_e32 v156, v0
	s_mov_b64 s[6:7], -1
	s_mov_b64 s[28:29], 0
	s_cmp_lt_i32 s66, 1
	s_mov_b64 s[0:1], 0
	s_cbranch_scc1 .LBB0_22
	s_cmp_eq_u32 s66, 1
	s_mov_b64 s[0:1], -1
	s_cbranch_scc0 .LBB0_26
	s_load_dwordx2 s[0:1], s[4:5], 0x130
	v_ashrrev_i32_e32 v157, 31, v156
	s_waitcnt lgkmcnt(0)
	s_barrier
	v_lshl_add_u64 v[20:21], v[156:157], 4, s[0:1]
	s_waitcnt vmcnt(0)
	v_add_co_u32_e32 v4, vcc, 0x1803d000, v20
	v_readlane_b32 s6, v253, 6
	s_nop 0
	v_addc_co_u32_e32 v5, vcc, 0, v21, vcc
	v_add_co_u32_e32 v8, vcc, 0x1803e000, v20
	v_add_u32_e32 v2, s6, v156
	s_nop 0
	v_addc_co_u32_e32 v9, vcc, 0, v21, vcc
	v_add_co_u32_e32 v12, vcc, 0x1803f000, v20
	global_load_dwordx4 v[4:7], v[4:5], off offset:256
	s_nop 0
	global_load_dwordx4 v[8:11], v[8:9], off offset:256
	v_addc_co_u32_e32 v13, vcc, 0, v21, vcc
	v_add_co_u32_e32 v16, vcc, 0x18040000, v20
	s_movk_i32 s6, 0x4400
	s_nop 0
	v_addc_co_u32_e32 v17, vcc, 0, v21, vcc
	v_add_co_u32_e32 v22, vcc, 0x18041000, v20
	global_load_dwordx4 v[12:15], v[12:13], off offset:256
	s_nop 0
	global_load_dwordx4 v[16:19], v[16:17], off offset:256
	v_addc_co_u32_e32 v23, vcc, 0, v21, vcc
	v_add_co_u32_e32 v26, vcc, 0x18042000, v20
	s_nop 1
	v_addc_co_u32_e32 v27, vcc, 0, v21, vcc
	v_add_co_u32_e32 v30, vcc, 0x18043000, v20
	global_load_dwordx4 v[22:25], v[22:23], off offset:256
	s_nop 0
	global_load_dwordx4 v[26:29], v[26:27], off offset:256
	v_addc_co_u32_e32 v31, vcc, 0, v21, vcc
	v_add_co_u32_e32 v20, vcc, 0x18044000, v20
	s_nop 1
	v_addc_co_u32_e32 v21, vcc, 0, v21, vcc
	global_load_dwordx4 v[30:33], v[30:31], off offset:256
	s_nop 0
	global_load_dwordx4 v[34:37], v[20:21], off offset:256
	v_ashrrev_i32_e32 v20, 6, v2
	v_lshlrev_b32_e32 v21, 4, v156
	v_cmp_gt_i32_e32 vcc, s6, v20
	s_waitcnt vmcnt(7)
	ds_write_b128 v21, v[4:7]
	s_waitcnt vmcnt(6)
	ds_write_b128 v21, v[8:11] offset:4096
	s_waitcnt vmcnt(5)
	ds_write_b128 v21, v[12:15] offset:8192
	s_waitcnt vmcnt(4)
	ds_write_b128 v21, v[16:19] offset:12288
	s_waitcnt vmcnt(3)
	ds_write_b128 v21, v[22:25] offset:16384
	s_waitcnt vmcnt(2)
	ds_write_b128 v21, v[26:29] offset:20480
	s_waitcnt vmcnt(1)
	ds_write_b128 v21, v[30:33] offset:24576
	s_waitcnt vmcnt(0)
	ds_write_b128 v21, v[34:37] offset:28672
	s_waitcnt lgkmcnt(0)
	s_barrier
	s_and_saveexec_b64 s[42:43], vcc
	s_cbranch_execz .LBB0_25
	s_load_dwordx2 s[6:7], s[4:5], 0x30
	v_and_b32_e32 v50, 63, v156
	v_lshlrev_b32_e32 v51, 4, v50
	v_cmp_lt_i32_e32 vcc, v229, v228
	s_add_u32 s44, s0, 0x100000
	s_waitcnt lgkmcnt(0)
	global_load_dwordx4 v[4:7], v51, s[6:7]
	global_load_dwordx4 v[8:11], v51, s[6:7] offset:1024
	global_load_dwordx4 v[12:15], v51, s[6:7] offset:2048
	global_load_dwordx4 v[16:19], v51, s[6:7] offset:3072
	v_cndmask_b32_e32 v21, v222, v229, vcc
	v_cmp_lt_i32_e32 vcc, v230, v228
	v_lshlrev_b32_e32 v52, 2, v21
	v_lshlrev_b32_e32 v2, 2, v50
	v_cndmask_b32_e32 v21, v222, v230, vcc
	v_cmp_lt_i32_e32 vcc, v231, v228
	v_lshlrev_b32_e32 v53, 2, v21
	v_lshlrev_b32_e32 v24, 3, v50
	v_cndmask_b32_e32 v21, v222, v231, vcc
	v_cmp_lt_i32_e32 vcc, v232, v228
	v_lshlrev_b32_e32 v54, 2, v21
	v_mov_b32_e32 v25, v3
	v_cndmask_b32_e32 v21, v222, v232, vcc
	v_cmp_lt_i32_e32 vcc, v233, v228
	v_lshlrev_b32_e32 v55, 2, v21
	s_addc_u32 s45, s1, 0
	v_cndmask_b32_e32 v21, v222, v233, vcc
	v_cmp_lt_i32_e32 vcc, v234, v228
	v_or_b32_e32 v28, 0x100, v2
	v_or_b32_e32 v30, 0x200, v2
	v_or_b32_e32 v32, 0x300, v2
	v_lshlrev_b32_e32 v56, 2, v21
	v_cndmask_b32_e32 v21, v222, v234, vcc
	v_lshl_add_u64 v[22:23], s[0:1], 0, v[2:3]
	s_mov_b64 s[6:7], 0x1034c000
	v_lshl_add_u64 v[24:25], s[0:1], 0, v[24:25]
	s_mov_b64 s[0:1], 0x45c6000
	v_lshlrev_b32_e32 v57, 2, v21
	v_cmp_gt_u32_e32 vcc, 8, v50
	v_lshl_add_u64 v[22:23], v[22:23], 0, s[6:7]
	v_lshl_add_u64 v[24:25], v[24:25], 0, s[0:1]
	s_mov_b64 s[46:47], 0
	v_lshlrev_b32_e32 v26, 2, v2
	v_lshlrev_b32_e32 v28, 2, v28
	v_lshlrev_b32_e32 v30, 2, v30
	v_lshlrev_b32_e32 v32, 2, v32
	v_mov_b32_e32 v27, v3
	v_mov_b32_e32 v29, v3
	v_mov_b32_e32 v31, v3
	v_mov_b32_e32 v33, v3
	s_load_dwordx2 s[98:99], s[4:5], 0x0
	s_load_dwordx2 s[100:101], s[4:5], 0x10
	s_waitcnt lgkmcnt(0)
	v_mov_b32_e32 v160, s98
	v_mov_b32_e32 v161, s99
	v_mov_b32_e32 v162, s100
	v_mov_b32_e32 v163, s101
	s_branch .LBB0_18

; __device__ __forceinline__ uint2 pack4(const f32x4 v) { uint2 o; o.x = pk2bf(v[0], v[1]); o.y = pk2bf(v[2], v[3]); return o; }
;     template <class T> __device__ __forceinline__ T* w(size_t off) const { return (T*)(p->ws + off); }
; __device__ __forceinline__ const float* xsrc(const Ctx& c, int layer, int n) {
;     if (layer == 0) { const int b = n / LT, pos = n % LT; return pos < CTX ? c.in(2) + ((size_t)b * CTX + pos) * D : c.in(0) + ((size_t)b * SEQ + (pos - CTX)) * D; }
;     return c.w<float>(WS_X) + (size_t)n * D;
; __device__ __forceinline__ void ph_norm1(const Ctx& c, int layer, int gw, int nwaves, unsigned char* lds) {
;     ...
;     for (int n = gw; n < NT; n += nwaves) {
;         const int b = n / LT, pos = n % LT, mr = pos < CTX ? 4 : b;
;         const float* x = xsrc(c, layer, n);
;         f32x4 v[4], sc[4], sh[4]; float ss = 0.f;
; #pragma unroll
;         for (int i = 0; i < 4; ++i) { const int k = (lane + 64 * i) * 4; v[i] = *(const f32x4*)(x + k); sc[i] = *(const f32x4*)(MOD + mr * 6144 + 1024 + k); sh[i] = *(const f32x4*)(MOD + mr * 6144 + k); }
; #pragma unroll
;         for (int i = 0; i < 4; ++i) ss += v[i][0] * v[i][0] + v[i][1] * v[i][1] + v[i][2] * v[i][2] + v[i][3] * v[i][3];
;         const float rstd = rsqrtf(wave_sum(ss) * (1.f / D) + EPS);
; #pragma unroll
;         for (int i = 0; i < 4; ++i) {
;             const int k = (lane + 64 * i) * 4;
;             v[i] = v[i] * rstd * gv[i] * (sc[i] + 1.f) + sh[i];
;             *(uint2*)(HA + (size_t)n * D + k) = pack4(v[i]);
;         }
;         dt_project(wdt, v, lane, DTR + (size_t)n * 8);
.LBB0_18:
	s_mov_b32 s0, 0x78787879
	v_mul_hi_i32 v2, v20, s0
	v_lshrrev_b32_e32 v21, 31, v2
	v_ashrrev_i32_e32 v2, 11, v2
	v_add_u32_e32 v34, v2, v21
	v_mul_i32_i24_e32 v2, 0x1100, v34
	v_sub_u32_e32 v21, v20, v2
	s_movk_i32 s0, 0x100
	v_cmp_gt_i32_e64 s[0:1], s0, v21
	v_ashrrev_i32_e32 v35, 31, v34
	v_add_u32_e32 v38, 0xffffff00, v21
	v_cndmask_b32_e64 v36, v160, v162, s[0:1]
	v_cndmask_b32_e64 v37, v161, v163, s[0:1]
	v_cndmask_b32_e64 v2, 24, 20, s[0:1]
	v_lshlrev_b64 v[40:41], v2, v[34:35]
	v_mul_i32_i24_e32 v2, 0x1800, v34
	v_ashrrev_i32_e32 v39, 31, v21
	v_cndmask_b32_e64 v34, v2, v235, s[0:1]
	v_cndmask_b32_e64 v39, 0, v39, s[0:1]
	v_cndmask_b32_e64 v38, v38, v21, s[0:1]
	v_ashrrev_i32_e32 v35, 31, v34
	v_lshlrev_b64 v[38:39], 12, v[38:39]
	v_lshl_add_u64 v[42:43], v[34:35], 2, s[44:45]
	s_mov_b64 s[0:1], 0x1000
	v_lshl_add_u64 v[82:83], v[42:43], 0, s[0:1]
	v_lshl_add_u64 v[86:87], v[42:43], 0, v[26:27]
	v_lshl_add_u64 v[58:59], v[82:83], 0, v[28:29]
	v_lshl_add_u64 v[70:71], v[82:83], 0, v[30:31]
	s_mov_b32 s6, 0
	v_lshl_add_u64 v[36:37], v[36:37], 0, v[40:41]
	v_lshl_add_u64 v[36:37], v[36:37], 0, v[38:39]
	v_lshl_add_u64 v[78:79], v[36:37], 0, v[26:27]
	v_lshl_add_u64 v[38:39], v[82:83], 0, v[26:27]
	global_load_dwordx4 v[34:37], v[78:79], off
	v_lshl_add_u64 v[82:83], v[82:83], 0, v[32:33]
	global_load_dwordx4 v[38:41], v[38:39], off
	s_nop 0
	global_load_dwordx4 v[42:45], v[86:87], off
	global_load_dwordx4 v[46:49], v[78:79], off offset:1024
	s_nop 0
	global_load_dwordx4 v[58:61], v[58:59], off
	s_nop 0
	global_load_dwordx4 v[62:65], v[86:87], off offset:1024
	global_load_dwordx4 v[66:69], v[78:79], off offset:2048
	s_nop 0
	global_load_dwordx4 v[70:73], v[70:71], off
	s_nop 0
	global_load_dwordx4 v[74:77], v[86:87], off offset:2048
	s_nop 0
	global_load_dwordx4 v[78:81], v[78:79], off offset:3072
	s_nop 0
	global_load_dwordx4 v[82:85], v[82:83], off
	s_nop 0
	global_load_dwordx4 v[86:89], v[86:87], off offset:3072
	s_waitcnt vmcnt(11)
	v_mov_b32_e32 v92, v35
	v_mov_b32_e32 v90, v34
	s_waitcnt vmcnt(10)
	v_pk_add_f32 v[38:39], v[38:39], 1.0 op_sel_hi:[1,0]
	s_waitcnt vmcnt(8)
	v_mov_b32_e32 v93, v47
	v_mov_b32_e32 v91, v46
	v_pk_mul_f32 v[92:93], v[92:93], v[92:93]
	s_waitcnt vmcnt(5)
	v_mov_b32_e32 v94, v67
	v_pk_fma_f32 v[90:91], v[90:91], v[90:91], v[92:93]
	v_mov_b32_e32 v92, v36
	v_mov_b32_e32 v93, v48
	v_pk_fma_f32 v[90:91], v[92:93], v[92:93], v[90:91]
	v_mov_b32_e32 v92, v37
	v_mov_b32_e32 v93, v49
	s_waitcnt vmcnt(2)
	v_mov_b32_e32 v95, v79
	v_pk_fma_f32 v[90:91], v[92:93], v[92:93], v[90:91]
	v_mov_b32_e32 v92, v66
	v_mov_b32_e32 v93, v78
	v_pk_mul_f32 v[94:95], v[94:95], v[94:95]
	v_add_f32_e32 v2, v90, v91
	v_pk_fma_f32 v[92:93], v[92:93], v[92:93], v[94:95]
	v_mov_b32_e32 v94, v68
	v_mov_b32_e32 v95, v80
	v_pk_fma_f32 v[92:93], v[94:95], v[94:95], v[92:93]
	v_mov_b32_e32 v94, v69
	v_mov_b32_e32 v95, v81
	v_pk_fma_f32 v[92:93], v[94:95], v[94:95], v[92:93]
	s_nop 0
	v_add_f32_e32 v2, v2, v92
	v_add_f32_e32 v2, v2, v93
	s_waitcnt lgkmcnt(0)
	s_nop 1
	v_add_f32_dpp v2, v2, v2 quad_perm:[1,0,3,2] row_mask:0xf bank_mask:0xf
	s_nop 1
	v_add_f32_dpp v2, v2, v2 quad_perm:[2,3,0,1] row_mask:0xf bank_mask:0xf
	s_nop 1
	v_add_f32_dpp v2, v2, v2 row_half_mirror row_mask:0xf bank_mask:0xf
	s_nop 1
	v_add_f32_dpp v2, v2, v2 row_mirror row_mask:0xf bank_mask:0xf
	v_mov_b32_e32 v21, v2
	s_nop 1
	v_permlane16_swap_b32_e32 v2, v21
	v_add_f32_e32 v2, v2, v21
	v_mov_b32_e32 v21, v2
	s_nop 1
	v_permlane32_swap_b32_e32 v2, v21
	v_add_f32_e32 v2, v2, v21
	v_fmamk_f32 v2, v2, 0x3a800000, v220
	v_cmp_gt_f32_e64 s[0:1], s91, v2
	v_mul_f32_e32 v21, 0x4b800000, v2
	s_nop 0
	v_cndmask_b32_e64 v2, v2, v21, s[0:1]
	v_rsq_f32_e32 v2, v2
	s_nop 0
	v_mul_f32_e32 v21, 0x45800000, v2
	v_cndmask_b32_e64 v2, v2, v21, s[0:1]
	v_pk_mul_f32 v[36:37], v[36:37], v[2:3] op_sel_hi:[1,0]
	v_pk_mul_f32 v[34:35], v[34:35], v[2:3] op_sel_hi:[1,0]
	v_ashrrev_i32_e32 v21, 31, v20
	v_pk_mul_f32 v[92:93], v[4:5], v[34:35]
	v_pk_mul_f32 v[34:35], v[6:7], v[36:37]
	v_pk_add_f32 v[36:37], v[40:41], 1.0 op_sel_hi:[1,0]
	v_lshlrev_b64 v[90:91], 11, v[20:21]
	v_pk_fma_f32 v[34:35], v[36:37], v[34:35], v[44:45]
	v_pk_fma_f32 v[92:93], v[38:39], v[92:93], v[42:43]
	v_cvt_pk_bf16_f32 v37, v34, v35
	v_cvt_pk_bf16_f32 v36, v92, v93
	v_lshl_add_u64 v[42:43], v[24:25], 0, v[90:91]
	global_store_dwordx2 v[42:43], v[36:37], off
	v_pk_mul_f32 v[36:37], v[48:49], v[2:3] op_sel_hi:[1,0]
	v_pk_mul_f32 v[38:39], v[46:47], v[2:3] op_sel_hi:[1,0]
	v_pk_mul_f32 v[36:37], v[10:11], v[36:37]
	v_pk_mul_f32 v[38:39], v[8:9], v[38:39]
	v_pk_add_f32 v[40:41], v[60:61], 1.0 op_sel_hi:[1,0]
	v_pk_add_f32 v[44:45], v[58:59], 1.0 op_sel_hi:[1,0]
	v_pk_fma_f32 v[48:49], v[40:41], v[36:37], v[64:65]
	v_pk_fma_f32 v[36:37], v[44:45], v[38:39], v[62:63]
	v_cvt_pk_bf16_f32 v39, v48, v49
	v_cvt_pk_bf16_f32 v38, v36, v37
	global_store_dwordx2 v[42:43], v[38:39], off offset:512
	v_pk_mul_f32 v[38:39], v[68:69], v[2:3] op_sel_hi:[1,0]
	v_pk_mul_f32 v[40:41], v[66:67], v[2:3] op_sel_hi:[1,0]
	v_pk_mul_f32 v[38:39], v[14:15], v[38:39]
	v_pk_mul_f32 v[40:41], v[12:13], v[40:41]
	v_pk_add_f32 v[44:45], v[72:73], 1.0 op_sel_hi:[1,0]
	v_pk_add_f32 v[46:47], v[70:71], 1.0 op_sel_hi:[1,0]
	v_pk_fma_f32 v[38:39], v[44:45], v[38:39], v[76:77]
	v_pk_fma_f32 v[46:47], v[46:47], v[40:41], v[74:75]
	v_cvt_pk_bf16_f32 v41, v38, v39
	v_cvt_pk_bf16_f32 v40, v46, v47
	global_store_dwordx2 v[42:43], v[40:41], off offset:1024
	v_pk_mul_f32 v[40:41], v[80:81], v[2:3] op_sel_hi:[1,0]
	v_pk_mul_f32 v[44:45], v[78:79], v[2:3] op_sel_hi:[1,0]
	v_pk_mul_f32 v[40:41], v[18:19], v[40:41]
	v_pk_mul_f32 v[44:45], v[16:17], v[44:45]
	s_waitcnt vmcnt(4)
	v_pk_add_f32 v[58:59], v[84:85], 1.0 op_sel_hi:[1,0]
	v_pk_add_f32 v[60:61], v[82:83], 1.0 op_sel_hi:[1,0]
	s_waitcnt vmcnt(3)
	v_pk_fma_f32 v[58:59], v[58:59], v[40:41], v[88:89]
	v_pk_fma_f32 v[40:41], v[60:61], v[44:45], v[86:87]
	v_cvt_pk_bf16_f32 v45, v58, v59
	v_cvt_pk_bf16_f32 v44, v40, v41
	global_store_dwordx2 v[42:43], v[44:45], off offset:1536
	v_mov_b32_e32 v42, v39
	v_mov_b32_e32 v43, v59
	v_mov_b32_e32 v39, v58
	v_mov_b32_e32 v44, v46
	v_mov_b32_e32 v45, v40
	v_mov_b32_e32 v40, v47
	v_mov_b32_e32 v46, v35
	v_mov_b32_e32 v47, v49
	v_mov_b32_e32 v35, v48
	v_mov_b32_e32 v48, v92
	v_mov_b32_e32 v49, v36
	v_mov_b32_e32 v36, v93
	v_mov_b32_e32 v58, 0
	v_mov_b32_e32 v2, v50
	v_mov_b32_e32 v59, v51
